# baseline (speedup 1.0000x reference)
_Z11prep_kernelPKfS0_PKiPDF16_S3_PfS4_:
	s_lshl_b32 s14, s2, 2
	v_lshrrev_b32_e32 v1, 8, v0
	v_or_b32_e32 v5, s14, v1
	s_movk_i32 s2, 0xff
	v_and_b32_e32 v4, 0xff, v0
	v_cmp_lt_i32_e32 vcc, s2, v5
	s_and_saveexec_b64 s[2:3], vcc
	s_xor_b64 s[2:3], exec, s[2:3]
	s_cbranch_execz .LBB0_5
	v_readfirstlane_b32 s15, v0
	s_and_b32 s17, s15, 0xff
	s_cmpk_ge_u32 s17, 0xc0
	s_cbranch_scc1 .LBB0_7
	s_load_dwordx4 s[8:11], s[0:1], 0x0
	s_load_dwordx4 s[4:7], s[0:1], 0x18
	v_add_u32_e32 v34, 0xffffff00, v5
	v_mov_b32_e32 v35, 0
	v_lshlrev_b64 v[32:33], 11, v[34:35]
	v_lshl_or_b32 v32, v4, 3, v32
	v_lshlrev_b64 v[0:1], 2, v[32:33]
	s_waitcnt lgkmcnt(0)
	s_cmp_lg_u32 s14, 0x100
	s_cbranch_scc1 .Lprep_noflag
	s_cmp_gt_u32 s15, 63
	s_cbranch_scc1 .Lprep_noflag
	s_add_u32 s16, s4, 0x3c08000
	s_addc_u32 s17, s5, 0
	v_lshlrev_b32_e32 v6, 2, v4
	v_mov_b32_e32 v7, 0
	v_mov_b32_e32 v8, s8
	v_mov_b32_e32 v9, s9
	v_mov_b32_e32 v10, s10
	v_mov_b32_e32 v11, s11
	global_store_dword v6, v7, s[16:17]
	global_store_dword v6, v7, s[16:17] offset:256
	global_store_dwordx4 v7, v[8:11], s[16:17] offset:2048

.LBB1_9:
	s_cmp_lt_i32 s56, 18
	s_cbranch_scc1 .Lqkv_nopoll
	s_cmp_gt_i32 s56, 24
	s_cbranch_scc1 .Lqkv_nopoll
	s_bitcmp1_b32 s56, 1
	s_cbranch_scc0 .Lqkv_chk
	s_sub_u32 s82, s56, 18
	s_lshl_b32 s82, s82, 6
	v_add_u32_e32 v242, s82, v241
	global_load_dword v240, v242, s[80:81] sc1
	s_branch .Lqkv_nopoll

.LBB1_30:
	s_and_b64 vcc, exec, s[4:5]
	s_cbranch_vccz .LBB1_41
	s_load_dwordx4 s[44:47], s[0:1], 0x0
	s_load_dwordx2 s[48:49], s[0:1], 0x20
	s_mov_b32 s50, s2
	v_and_b32_e32 v1, 31, v0
	v_lshrrev_b32_e32 v2, 5, v0
	v_lshlrev_b32_e32 v3, 5, v1
	v_lshl_add_u32 v3, v2, 13, v3
	v_add_u32_e32 v3, 0x1800, v3
	v_lshlrev_b32_e32 v4, 4, v1
	v_lshl_add_u32 v4, v2, 12, v4
	v_add_u32_e32 v4, 0xc00, v4
	s_waitcnt lgkmcnt(0)
	s_add_u32 s48, s48, 0x408000
	s_addc_u32 s49, s49, 0
	s_load_dwordx4 s[52:55], s[48:49], 0x800
	s_lshl_b32 s51, s50, 18
	s_add_u32 s44, s44, s51
	s_addc_u32 s45, s45, 0
	s_mul_i32 s51, s50, 0x30000
	s_add_u32 s46, s46, s51
	s_addc_u32 s47, s47, 0
	s_waitcnt lgkmcnt(0)
	s_lshl_b32 s51, s50, 19
	s_add_u32 s52, s52, s51
	s_addc_u32 s53, s53, 0
	s_mul_i32 s51, s50, 0x60000
	s_add_u32 s54, s54, s51
	s_addc_u32 s55, s55, 0
	v_cmp_eq_u32_e64 s[78:79], 0, v0
	v_mov_b32_e32 v5, 1
	v_mov_b32_e32 v6, s50
	v_lshlrev_b32_e32 v6, 2, v6
	s_add_u32 s58, s52, 0x0
	s_addc_u32 s59, s53, 0
	global_load_dwordx4 v[16:19], v3, s[58:59] nt
	global_load_dwordx4 v[20:23], v3, s[58:59] offset:16 nt
	s_add_u32 s58, s52, 0x20000
	s_addc_u32 s59, s53, 0
	global_load_dwordx4 v[24:27], v3, s[58:59] nt
	global_load_dwordx4 v[28:31], v3, s[58:59] offset:16 nt
	s_add_u32 s58, s52, 0x40000
	s_addc_u32 s59, s53, 0
	global_load_dwordx4 v[32:35], v3, s[58:59] nt
	global_load_dwordx4 v[36:39], v3, s[58:59] offset:16 nt
	s_add_u32 s58, s52, 0x60000
	s_addc_u32 s59, s53, 0
	global_load_dwordx4 v[40:43], v3, s[58:59] nt
	global_load_dwordx4 v[44:47], v3, s[58:59] offset:16 nt
	s_add_u32 s58, s54, 0x0
	s_addc_u32 s59, s55, 0
	global_load_dwordx4 v[48:51], v3, s[58:59] nt
	global_load_dwordx4 v[52:55], v3, s[58:59] offset:16 nt
	s_add_u32 s58, s54, 0x20000
	s_addc_u32 s59, s55, 0
	global_load_dwordx4 v[56:59], v3, s[58:59] nt
	global_load_dwordx4 v[60:63], v3, s[58:59] offset:16 nt
	s_add_u32 s58, s54, 0x40000
	s_addc_u32 s59, s55, 0
	global_load_dwordx4 v[64:67], v3, s[58:59] nt
	global_load_dwordx4 v[68:71], v3, s[58:59] offset:16 nt
	s_add_u32 s58, s52, 0x400
	s_addc_u32 s59, s53, 0
	global_load_dwordx4 v[72:75], v3, s[58:59] nt
	global_load_dwordx4 v[76:79], v3, s[58:59] offset:16 nt
	s_add_u32 s58, s52, 0x20400
	s_addc_u32 s59, s53, 0
	global_load_dwordx4 v[80:83], v3, s[58:59] nt
	global_load_dwordx4 v[84:87], v3, s[58:59] offset:16 nt
	s_add_u32 s58, s52, 0x40400
	s_addc_u32 s59, s53, 0
	global_load_dwordx4 v[88:91], v3, s[58:59] nt
	global_load_dwordx4 v[92:95], v3, s[58:59] offset:16 nt
	s_add_u32 s58, s52, 0x60400
	s_addc_u32 s59, s53, 0
	global_load_dwordx4 v[96:99], v3, s[58:59] nt
	global_load_dwordx4 v[100:103], v3, s[58:59] offset:16 nt
	s_add_u32 s58, s54, 0x400
	s_addc_u32 s59, s55, 0
	global_load_dwordx4 v[104:107], v3, s[58:59] nt
	global_load_dwordx4 v[108:111], v3, s[58:59] offset:16 nt
	s_add_u32 s58, s54, 0x20400
	s_addc_u32 s59, s55, 0
	global_load_dwordx4 v[112:115], v3, s[58:59] nt
	global_load_dwordx4 v[116:119], v3, s[58:59] offset:16 nt
	s_add_u32 s58, s54, 0x40400
	s_addc_u32 s59, s55, 0
	global_load_dwordx4 v[120:123], v3, s[58:59] nt
	global_load_dwordx4 v[124:127], v3, s[58:59] offset:16 nt
	s_waitcnt vmcnt(26)
	v_cvt_pk_f16_f32 v16, v16, v17
	v_cvt_pk_f16_f32 v17, v18, v19
	v_cvt_pk_f16_f32 v18, v20, v21
	v_cvt_pk_f16_f32 v19, v22, v23
	s_add_u32 s76, s44, 0x0
	s_addc_u32 s77, s45, 0
	global_store_dwordx4 v4, v[16:19], s[76:77] sc1
	s_waitcnt vmcnt(25)
	v_cvt_pk_f16_f32 v24, v24, v25
	v_cvt_pk_f16_f32 v25, v26, v27
	v_cvt_pk_f16_f32 v26, v28, v29
	v_cvt_pk_f16_f32 v27, v30, v31
	s_add_u32 s76, s44, 0x10000
	s_addc_u32 s77, s45, 0
	global_store_dwordx4 v4, v[24:27], s[76:77] sc1
	s_waitcnt vmcnt(24)
	v_cvt_pk_f16_f32 v32, v32, v33
	v_cvt_pk_f16_f32 v33, v34, v35
	v_cvt_pk_f16_f32 v34, v36, v37
	v_cvt_pk_f16_f32 v35, v38, v39
	s_add_u32 s76, s44, 0x20000
	s_addc_u32 s77, s45, 0
	global_store_dwordx4 v4, v[32:35], s[76:77] sc1
	s_waitcnt vmcnt(23)
	v_cvt_pk_f16_f32 v40, v40, v41
	v_cvt_pk_f16_f32 v41, v42, v43
	v_cvt_pk_f16_f32 v42, v44, v45
	v_cvt_pk_f16_f32 v43, v46, v47
	s_add_u32 s76, s44, 0x30000
	s_addc_u32 s77, s45, 0
	global_store_dwordx4 v4, v[40:43], s[76:77] sc1
	s_waitcnt vmcnt(22)
	v_cvt_pk_f16_f32 v48, v48, v49
	v_cvt_pk_f16_f32 v49, v50, v51
	v_cvt_pk_f16_f32 v50, v52, v53
	v_cvt_pk_f16_f32 v51, v54, v55
	s_add_u32 s76, s46, 0x0
	s_addc_u32 s77, s47, 0
	global_store_dwordx4 v4, v[48:51], s[76:77] sc1
	s_waitcnt vmcnt(21)
	v_cvt_pk_f16_f32 v56, v56, v57
	v_cvt_pk_f16_f32 v57, v58, v59
	v_cvt_pk_f16_f32 v58, v60, v61
	v_cvt_pk_f16_f32 v59, v62, v63
	s_add_u32 s76, s46, 0x10000
	s_addc_u32 s77, s47, 0
	global_store_dwordx4 v4, v[56:59], s[76:77] sc1
	s_waitcnt vmcnt(20)
	v_cvt_pk_f16_f32 v64, v64, v65
	v_cvt_pk_f16_f32 v65, v66, v67
	v_cvt_pk_f16_f32 v66, v68, v69
	v_cvt_pk_f16_f32 v67, v70, v71
	s_add_u32 s76, s46, 0x20000
	s_addc_u32 s77, s47, 0
	global_store_dwordx4 v4, v[64:67], s[76:77] sc1
	s_waitcnt vmcnt(19)
	v_cvt_pk_f16_f32 v72, v72, v73
	v_cvt_pk_f16_f32 v73, v74, v75
	v_cvt_pk_f16_f32 v74, v76, v77
	v_cvt_pk_f16_f32 v75, v78, v79
	s_add_u32 s76, s44, 0x200
	s_addc_u32 s77, s45, 0
	global_store_dwordx4 v4, v[72:75], s[76:77] sc1
	s_waitcnt vmcnt(18)
	v_cvt_pk_f16_f32 v80, v80, v81
	v_cvt_pk_f16_f32 v81, v82, v83
	v_cvt_pk_f16_f32 v82, v84, v85
	v_cvt_pk_f16_f32 v83, v86, v87
	s_add_u32 s76, s44, 0x10200
	s_addc_u32 s77, s45, 0
	global_store_dwordx4 v4, v[80:83], s[76:77] sc1
	s_waitcnt vmcnt(17)
	v_cvt_pk_f16_f32 v88, v88, v89
	v_cvt_pk_f16_f32 v89, v90, v91
	v_cvt_pk_f16_f32 v90, v92, v93
	v_cvt_pk_f16_f32 v91, v94, v95
	s_add_u32 s76, s44, 0x20200
	s_addc_u32 s77, s45, 0
	global_store_dwordx4 v4, v[88:91], s[76:77] sc1
	s_waitcnt vmcnt(16)
	v_cvt_pk_f16_f32 v96, v96, v97
	v_cvt_pk_f16_f32 v97, v98, v99
	v_cvt_pk_f16_f32 v98, v100, v101
	v_cvt_pk_f16_f32 v99, v102, v103
	s_add_u32 s76, s44, 0x30200
	s_addc_u32 s77, s45, 0
	global_store_dwordx4 v4, v[96:99], s[76:77] sc1
	s_waitcnt vmcnt(15)
	v_cvt_pk_f16_f32 v104, v104, v105
	v_cvt_pk_f16_f32 v105, v106, v107
	v_cvt_pk_f16_f32 v106, v108, v109
	v_cvt_pk_f16_f32 v107, v110, v111
	s_add_u32 s76, s46, 0x200
	s_addc_u32 s77, s47, 0
	global_store_dwordx4 v4, v[104:107], s[76:77] sc1
	s_waitcnt vmcnt(14)
	v_cvt_pk_f16_f32 v112, v112, v113
	v_cvt_pk_f16_f32 v113, v114, v115
	v_cvt_pk_f16_f32 v114, v116, v117
	v_cvt_pk_f16_f32 v115, v118, v119
	s_add_u32 s76, s46, 0x10200
	s_addc_u32 s77, s47, 0
	global_store_dwordx4 v4, v[112:115], s[76:77] sc1
	s_waitcnt vmcnt(13)
	v_cvt_pk_f16_f32 v120, v120, v121
	v_cvt_pk_f16_f32 v121, v122, v123
	v_cvt_pk_f16_f32 v122, v124, v125
	v_cvt_pk_f16_f32 v123, v126, v127
	s_add_u32 s76, s46, 0x20200
	s_addc_u32 s77, s47, 0
	global_store_dwordx4 v4, v[120:123], s[76:77] sc1
	s_waitcnt vmcnt(7)
	s_barrier
	s_mov_b64 s[56:57], exec
	s_and_b64 exec, exec, s[78:79]
	global_store_dword v6, v5, s[48:49] offset:0 sc1
	s_mov_b64 exec, s[56:57]
	s_waitcnt vmcnt(1)
	s_barrier
	s_mov_b64 s[56:57], exec
	s_and_b64 exec, exec, s[78:79]
	global_store_dword v6, v5, s[48:49] offset:256 sc1
	s_mov_b64 exec, s[56:57]
	s_mov_b32 s24, s2
	s_lshl_b32 s20, s24, 4
	s_lshl_b32 s0, s24, 5
	s_ashr_i32 s21, s20, 31
	s_and_b32 s25, s0, 0xffffffc0
	s_lshl_b64 s[20:21], s[20:21], 2
	v_lshrrev_b32_e32 v6, 6, v0
	s_waitcnt lgkmcnt(0)
	s_add_u32 s26, s30, s20
	s_addc_u32 s27, s31, s21
	v_lshl_or_b32 v2, v6, 3, s25
	s_and_b32 s25, s2, 1
	s_lshl_b32 s2, s25, 7
	s_add_u32 s20, s28, s2
	v_and_b32_e32 v7, 63, v0
	s_mov_b32 s3, 0
	s_addc_u32 s21, s29, 0
	s_bfe_u32 s2, s24, 0x1a0001
	v_add_u32_e32 v2, v2, v7
	v_mov_b32_e32 v3, 0
	s_lshl_b64 s[2:3], s[2:3], 19
	v_lshl_add_u32 v1, v6, 2, 0
	v_lshlrev_b64 v[4:5], 8, v[2:3]
	v_lshl_or_b32 v2, v6, 16, s2
	s_lshl_b32 s2, s25, 12
	v_lshlrev_b32_e32 v6, 2, v7
	v_cmp_gt_u32_e64 s[0:1], 8, v7
	v_cmp_eq_u32_e64 s[22:23], 0, v7
	v_cmp_eq_u32_e64 s[6:7], 1, v7
	v_cmp_eq_u32_e64 s[8:9], 2, v7
	v_cmp_eq_u32_e64 s[10:11], 3, v7
	v_cmp_eq_u32_e64 s[12:13], 4, v7
	v_cmp_eq_u32_e64 s[14:15], 5, v7
	v_cmp_eq_u32_e64 s[16:17], 6, v7
	v_cmp_eq_u32_e64 s[18:19], 7, v7
	v_or3_b32 v6, v2, s2, v6
	v_mov_b32_e32 v7, s3
	v_cmp_eq_u32_e64 s[4:5], 0, v0
	v_lshl_add_u64 v[4:5], s[20:21], 0, v[4:5]
	v_lshl_add_u64 v[6:7], s[42:43], 0, v[6:7]
	s_mov_b64 s[28:29], 0
	s_lshr_b32 s58, s24, 1
	s_lshl_b32 s58, s58, 19
	s_add_u32 s60, s42, s58
	s_addc_u32 s61, s43, 0
	s_add_u32 s62, s60, 0x2000
	s_addc_u32 s63, s61, 0
	s_add_u32 s64, s62, 0x2000
	s_addc_u32 s65, s63, 0
	s_add_u32 s66, s64, 0x2000
	s_addc_u32 s67, s65, 0
	s_add_u32 s68, s66, 0x2000
	s_addc_u32 s69, s67, 0
	s_add_u32 s70, s68, 0x2000
	s_addc_u32 s71, s69, 0
	s_add_u32 s72, s70, 0x2000
	s_addc_u32 s73, s71, 0
	s_add_u32 s74, s72, 0x2000
	s_addc_u32 s75, s73, 0
	v_lshrrev_b32_e32 v96, 6, v0
	v_lshlrev_b32_e32 v96, 16, v96
	v_and_b32_e32 v97, 63, v0
	v_lshl_add_u32 v96, v97, 2, v96
	s_and_b32 s59, s24, 1
	s_lshl_b32 s59, s59, 12
	v_add_u32_e32 v96, s59, v96
	s_mov_b32 s76, 0
	s_mov_b32 s77, 0
	global_load_dword v100, v96, s[60:61] offset:0 nt
	global_load_dword v101, v96, s[62:63] offset:0 nt
	global_load_dword v102, v96, s[64:65] offset:0 nt
	global_load_dword v103, v96, s[66:67] offset:0 nt
	global_load_dword v104, v96, s[68:69] offset:0 nt
	global_load_dword v105, v96, s[70:71] offset:0 nt
	global_load_dword v106, v96, s[72:73] offset:0 nt
	global_load_dword v107, v96, s[74:75] offset:0 nt
	global_load_dword v108, v96, s[60:61] offset:256 nt
	global_load_dword v109, v96, s[62:63] offset:256 nt
	global_load_dword v110, v96, s[64:65] offset:256 nt
	global_load_dword v111, v96, s[66:67] offset:256 nt
	global_load_dword v112, v96, s[68:69] offset:256 nt
	global_load_dword v113, v96, s[70:71] offset:256 nt
	global_load_dword v114, v96, s[72:73] offset:256 nt
	global_load_dword v115, v96, s[74:75] offset:256 nt
	global_load_dword v116, v96, s[60:61] offset:512 nt
	global_load_dword v117, v96, s[62:63] offset:512 nt
	global_load_dword v118, v96, s[64:65] offset:512 nt
	global_load_dword v119, v96, s[66:67] offset:512 nt
	global_load_dword v120, v96, s[68:69] offset:512 nt
	global_load_dword v121, v96, s[70:71] offset:512 nt
	global_load_dword v122, v96, s[72:73] offset:512 nt
	global_load_dword v123, v96, s[74:75] offset:512 nt
	global_load_dword v124, v96, s[60:61] offset:768 nt
	global_load_dword v125, v96, s[62:63] offset:768 nt
	global_load_dword v126, v96, s[64:65] offset:768 nt
	global_load_dword v127, v96, s[66:67] offset:768 nt
	global_load_dword v128, v96, s[68:69] offset:768 nt
	global_load_dword v129, v96, s[70:71] offset:768 nt
	global_load_dword v130, v96, s[72:73] offset:768 nt
	global_load_dword v131, v96, s[74:75] offset:768 nt
	global_load_dword v132, v96, s[60:61] offset:1024 nt
	global_load_dword v133, v96, s[62:63] offset:1024 nt
	global_load_dword v134, v96, s[64:65] offset:1024 nt
	global_load_dword v135, v96, s[66:67] offset:1024 nt
	global_load_dword v136, v96, s[68:69] offset:1024 nt
	global_load_dword v137, v96, s[70:71] offset:1024 nt
	global_load_dword v138, v96, s[72:73] offset:1024 nt
	global_load_dword v139, v96, s[74:75] offset:1024 nt
	global_load_dword v140, v96, s[60:61] offset:1280 nt
	global_load_dword v141, v96, s[62:63] offset:1280 nt
	global_load_dword v142, v96, s[64:65] offset:1280 nt
	global_load_dword v143, v96, s[66:67] offset:1280 nt
	global_load_dword v144, v96, s[68:69] offset:1280 nt
	global_load_dword v145, v96, s[70:71] offset:1280 nt
	global_load_dword v146, v96, s[72:73] offset:1280 nt
	global_load_dword v147, v96, s[74:75] offset:1280 nt
	global_load_dword v148, v96, s[60:61] offset:1536 nt
	global_load_dword v149, v96, s[62:63] offset:1536 nt
	global_load_dword v150, v96, s[64:65] offset:1536 nt
	global_load_dword v151, v96, s[66:67] offset:1536 nt
	global_load_dword v152, v96, s[68:69] offset:1536 nt
	global_load_dword v153, v96, s[70:71] offset:1536 nt
	global_load_dword v154, v96, s[72:73] offset:1536 nt
	global_load_dword v155, v96, s[74:75] offset:1536 nt
	s_waitcnt vmcnt(48)
	v_cmp_ne_u32_e32 vcc, 0, v100
	s_nop 1
	v_mov_b32_e32 v2, vcc_lo
	v_mov_b32_e32 v9, vcc_hi
	v_cmp_ne_u32_e32 vcc, 0, v101
	v_cndmask_b32_e64 v2, 0, v2, s[22:23]
	v_cndmask_b32_e64 v9, 0, v9, s[22:23]
	v_mov_b32_e32 v11, vcc_hi
	v_mov_b32_e32 v14, vcc_lo
	v_cndmask_b32_e64 v9, v9, v11, s[6:7]
	v_cndmask_b32_e64 v2, v2, v14, s[6:7]
	v_cmp_ne_u32_e32 vcc, 0, v102
	s_nop 1
	v_mov_b32_e32 v11, vcc_lo
	v_mov_b32_e32 v14, vcc_hi
	v_cmp_ne_u32_e32 vcc, 0, v103
	v_cndmask_b32_e64 v2, v2, v11, s[8:9]
	v_cndmask_b32_e64 v9, v9, v14, s[8:9]
	v_mov_b32_e32 v11, vcc_hi
	v_mov_b32_e32 v14, vcc_lo
	v_cmp_ne_u32_e32 vcc, 0, v104
	v_cndmask_b32_e64 v9, v9, v11, s[10:11]
	v_cndmask_b32_e64 v2, v2, v14, s[10:11]
	v_mov_b32_e32 v11, vcc_lo
	v_mov_b32_e32 v12, vcc_hi
	v_cmp_ne_u32_e32 vcc, 0, v105
	v_cndmask_b32_e64 v2, v2, v11, s[12:13]
	v_cndmask_b32_e64 v9, v9, v12, s[12:13]
	v_mov_b32_e32 v11, vcc_hi
	v_mov_b32_e32 v12, vcc_lo
	v_cndmask_b32_e64 v9, v9, v11, s[14:15]
	v_cndmask_b32_e64 v2, v2, v12, s[14:15]
	v_cmp_ne_u32_e32 vcc, 0, v106
	s_nop 1
	v_mov_b32_e32 v10, vcc_lo
	v_mov_b32_e32 v11, vcc_hi
	v_cmp_ne_u32_e32 vcc, 0, v107
	v_cndmask_b32_e64 v2, v2, v10, s[16:17]
	v_cndmask_b32_e64 v8, v9, v11, s[16:17]
	v_mov_b32_e32 v9, vcc_hi
	v_mov_b32_e32 v10, vcc_lo
	v_cndmask_b32_e64 v9, v8, v9, s[18:19]
	v_cndmask_b32_e64 v8, v2, v10, s[18:19]
	s_mov_b64 s[2:3], exec
	s_mov_b64 exec, s[0:1]
	global_store_dwordx2 v[4:5], v[8:9], off
	s_mov_b64 exec, s[2:3]
	v_cmp_ne_u64_e32 vcc, 0, v[8:9]
	s_and_b64 s[20:21], s[0:1], vcc
	s_cmp_lg_u64 s[20:21], 0
	s_cselect_b32 s20, 1, 0
	s_or_b32 s76, s76, s20
	v_cmp_ne_u64_e32 vcc, -1, v[8:9]
	s_and_b64 s[20:21], s[0:1], vcc
	s_cmp_lg_u64 s[20:21], 0
	s_cselect_b32 s20, 1, 0
	s_or_b32 s77, s77, s20
	v_lshl_add_u64 v[4:5], v[4:5], 0, 8
	global_load_dword v156, v96, s[60:61] offset:1792 nt
	global_load_dword v157, v96, s[62:63] offset:1792 nt
	global_load_dword v158, v96, s[64:65] offset:1792 nt
	global_load_dword v159, v96, s[66:67] offset:1792 nt
	global_load_dword v160, v96, s[68:69] offset:1792 nt
	global_load_dword v161, v96, s[70:71] offset:1792 nt
	global_load_dword v162, v96, s[72:73] offset:1792 nt
	global_load_dword v163, v96, s[74:75] offset:1792 nt
	s_waitcnt vmcnt(49)
	v_cmp_ne_u32_e32 vcc, 0, v108
	s_nop 1
	v_mov_b32_e32 v2, vcc_lo
	v_mov_b32_e32 v9, vcc_hi
	v_cmp_ne_u32_e32 vcc, 0, v109
	v_cndmask_b32_e64 v2, 0, v2, s[22:23]
	v_cndmask_b32_e64 v9, 0, v9, s[22:23]
	v_mov_b32_e32 v11, vcc_hi
	v_mov_b32_e32 v14, vcc_lo
	v_cndmask_b32_e64 v9, v9, v11, s[6:7]
	v_cndmask_b32_e64 v2, v2, v14, s[6:7]
	v_cmp_ne_u32_e32 vcc, 0, v110
	s_nop 1
	v_mov_b32_e32 v11, vcc_lo
	v_mov_b32_e32 v14, vcc_hi
	v_cmp_ne_u32_e32 vcc, 0, v111
	v_cndmask_b32_e64 v2, v2, v11, s[8:9]
	v_cndmask_b32_e64 v9, v9, v14, s[8:9]
	v_mov_b32_e32 v11, vcc_hi
	v_mov_b32_e32 v14, vcc_lo
	v_cmp_ne_u32_e32 vcc, 0, v112
	v_cndmask_b32_e64 v9, v9, v11, s[10:11]
	v_cndmask_b32_e64 v2, v2, v14, s[10:11]
	v_mov_b32_e32 v11, vcc_lo
	v_mov_b32_e32 v12, vcc_hi
	v_cmp_ne_u32_e32 vcc, 0, v113
	v_cndmask_b32_e64 v2, v2, v11, s[12:13]
	v_cndmask_b32_e64 v9, v9, v12, s[12:13]
	v_mov_b32_e32 v11, vcc_hi
	v_mov_b32_e32 v12, vcc_lo
	v_cndmask_b32_e64 v9, v9, v11, s[14:15]
	v_cndmask_b32_e64 v2, v2, v12, s[14:15]
	v_cmp_ne_u32_e32 vcc, 0, v114
	s_nop 1
	v_mov_b32_e32 v10, vcc_lo
	v_mov_b32_e32 v11, vcc_hi
	v_cmp_ne_u32_e32 vcc, 0, v115
	v_cndmask_b32_e64 v2, v2, v10, s[16:17]
	v_cndmask_b32_e64 v8, v9, v11, s[16:17]
	v_mov_b32_e32 v9, vcc_hi
	v_mov_b32_e32 v10, vcc_lo
	v_cndmask_b32_e64 v9, v8, v9, s[18:19]
	v_cndmask_b32_e64 v8, v2, v10, s[18:19]
	s_mov_b64 s[2:3], exec
	s_mov_b64 exec, s[0:1]
	global_store_dwordx2 v[4:5], v[8:9], off
	s_mov_b64 exec, s[2:3]
	v_cmp_ne_u64_e32 vcc, 0, v[8:9]
	s_and_b64 s[20:21], s[0:1], vcc
	s_cmp_lg_u64 s[20:21], 0
	s_cselect_b32 s20, 2, 0
	s_or_b32 s76, s76, s20
	v_cmp_ne_u64_e32 vcc, -1, v[8:9]
	s_and_b64 s[20:21], s[0:1], vcc
	s_cmp_lg_u64 s[20:21], 0
	s_cselect_b32 s20, 2, 0
	s_or_b32 s77, s77, s20
	v_lshl_add_u64 v[4:5], v[4:5], 0, 8
	global_load_dword v164, v96, s[60:61] offset:2048 nt
	global_load_dword v165, v96, s[62:63] offset:2048 nt
	global_load_dword v166, v96, s[64:65] offset:2048 nt
	global_load_dword v167, v96, s[66:67] offset:2048 nt
	global_load_dword v168, v96, s[68:69] offset:2048 nt
	global_load_dword v169, v96, s[70:71] offset:2048 nt
	global_load_dword v170, v96, s[72:73] offset:2048 nt
	global_load_dword v171, v96, s[74:75] offset:2048 nt
	s_waitcnt vmcnt(50)
	v_cmp_ne_u32_e32 vcc, 0, v116
	s_nop 1
	v_mov_b32_e32 v2, vcc_lo
	v_mov_b32_e32 v9, vcc_hi
	v_cmp_ne_u32_e32 vcc, 0, v117
	v_cndmask_b32_e64 v2, 0, v2, s[22:23]
	v_cndmask_b32_e64 v9, 0, v9, s[22:23]
	v_mov_b32_e32 v11, vcc_hi
	v_mov_b32_e32 v14, vcc_lo
	v_cndmask_b32_e64 v9, v9, v11, s[6:7]
	v_cndmask_b32_e64 v2, v2, v14, s[6:7]
	v_cmp_ne_u32_e32 vcc, 0, v118
	s_nop 1
	v_mov_b32_e32 v11, vcc_lo
	v_mov_b32_e32 v14, vcc_hi
	v_cmp_ne_u32_e32 vcc, 0, v119
	v_cndmask_b32_e64 v2, v2, v11, s[8:9]
	v_cndmask_b32_e64 v9, v9, v14, s[8:9]
	v_mov_b32_e32 v11, vcc_hi
	v_mov_b32_e32 v14, vcc_lo
	v_cmp_ne_u32_e32 vcc, 0, v120
	v_cndmask_b32_e64 v9, v9, v11, s[10:11]
	v_cndmask_b32_e64 v2, v2, v14, s[10:11]
	v_mov_b32_e32 v11, vcc_lo
	v_mov_b32_e32 v12, vcc_hi
	v_cmp_ne_u32_e32 vcc, 0, v121
	v_cndmask_b32_e64 v2, v2, v11, s[12:13]
	v_cndmask_b32_e64 v9, v9, v12, s[12:13]
	v_mov_b32_e32 v11, vcc_hi
	v_mov_b32_e32 v12, vcc_lo
	v_cndmask_b32_e64 v9, v9, v11, s[14:15]
	v_cndmask_b32_e64 v2, v2, v12, s[14:15]
	v_cmp_ne_u32_e32 vcc, 0, v122
	s_nop 1
	v_mov_b32_e32 v10, vcc_lo
	v_mov_b32_e32 v11, vcc_hi
	v_cmp_ne_u32_e32 vcc, 0, v123
	v_cndmask_b32_e64 v2, v2, v10, s[16:17]
	v_cndmask_b32_e64 v8, v9, v11, s[16:17]
	v_mov_b32_e32 v9, vcc_hi
	v_mov_b32_e32 v10, vcc_lo
	v_cndmask_b32_e64 v9, v8, v9, s[18:19]
	v_cndmask_b32_e64 v8, v2, v10, s[18:19]
	s_mov_b64 s[2:3], exec
	s_mov_b64 exec, s[0:1]
	global_store_dwordx2 v[4:5], v[8:9], off
	s_mov_b64 exec, s[2:3]
	v_cmp_ne_u64_e32 vcc, 0, v[8:9]
	s_and_b64 s[20:21], s[0:1], vcc
	s_cmp_lg_u64 s[20:21], 0
	s_cselect_b32 s20, 4, 0
	s_or_b32 s76, s76, s20
	v_cmp_ne_u64_e32 vcc, -1, v[8:9]
	s_and_b64 s[20:21], s[0:1], vcc
	s_cmp_lg_u64 s[20:21], 0
	s_cselect_b32 s20, 4, 0
	s_or_b32 s77, s77, s20
	v_lshl_add_u64 v[4:5], v[4:5], 0, 8
	global_load_dword v172, v96, s[60:61] offset:2304 nt
	global_load_dword v173, v96, s[62:63] offset:2304 nt
	global_load_dword v174, v96, s[64:65] offset:2304 nt
	global_load_dword v175, v96, s[66:67] offset:2304 nt
	global_load_dword v176, v96, s[68:69] offset:2304 nt
	global_load_dword v177, v96, s[70:71] offset:2304 nt
	global_load_dword v178, v96, s[72:73] offset:2304 nt
	global_load_dword v179, v96, s[74:75] offset:2304 nt
	s_waitcnt vmcnt(51)
	v_cmp_ne_u32_e32 vcc, 0, v124
	s_nop 1
	v_mov_b32_e32 v2, vcc_lo
	v_mov_b32_e32 v9, vcc_hi
	v_cmp_ne_u32_e32 vcc, 0, v125
	v_cndmask_b32_e64 v2, 0, v2, s[22:23]
	v_cndmask_b32_e64 v9, 0, v9, s[22:23]
	v_mov_b32_e32 v11, vcc_hi
	v_mov_b32_e32 v14, vcc_lo
	v_cndmask_b32_e64 v9, v9, v11, s[6:7]
	v_cndmask_b32_e64 v2, v2, v14, s[6:7]
	v_cmp_ne_u32_e32 vcc, 0, v126
	s_nop 1
	v_mov_b32_e32 v11, vcc_lo
	v_mov_b32_e32 v14, vcc_hi
	v_cmp_ne_u32_e32 vcc, 0, v127
	v_cndmask_b32_e64 v2, v2, v11, s[8:9]
	v_cndmask_b32_e64 v9, v9, v14, s[8:9]
	v_mov_b32_e32 v11, vcc_hi
	v_mov_b32_e32 v14, vcc_lo
	v_cmp_ne_u32_e32 vcc, 0, v128
	v_cndmask_b32_e64 v9, v9, v11, s[10:11]
	v_cndmask_b32_e64 v2, v2, v14, s[10:11]
	v_mov_b32_e32 v11, vcc_lo
	v_mov_b32_e32 v12, vcc_hi
	v_cmp_ne_u32_e32 vcc, 0, v129
	v_cndmask_b32_e64 v2, v2, v11, s[12:13]
	v_cndmask_b32_e64 v9, v9, v12, s[12:13]
	v_mov_b32_e32 v11, vcc_hi
	v_mov_b32_e32 v12, vcc_lo
	v_cndmask_b32_e64 v9, v9, v11, s[14:15]
	v_cndmask_b32_e64 v2, v2, v12, s[14:15]
	v_cmp_ne_u32_e32 vcc, 0, v130
	s_nop 1
	v_mov_b32_e32 v10, vcc_lo
	v_mov_b32_e32 v11, vcc_hi
	v_cmp_ne_u32_e32 vcc, 0, v131
	v_cndmask_b32_e64 v2, v2, v10, s[16:17]
	v_cndmask_b32_e64 v8, v9, v11, s[16:17]
	v_mov_b32_e32 v9, vcc_hi
	v_mov_b32_e32 v10, vcc_lo
	v_cndmask_b32_e64 v9, v8, v9, s[18:19]
	v_cndmask_b32_e64 v8, v2, v10, s[18:19]
	s_mov_b64 s[2:3], exec
	s_mov_b64 exec, s[0:1]
	global_store_dwordx2 v[4:5], v[8:9], off
	s_mov_b64 exec, s[2:3]
	v_cmp_ne_u64_e32 vcc, 0, v[8:9]
	s_and_b64 s[20:21], s[0:1], vcc
	s_cmp_lg_u64 s[20:21], 0
	s_cselect_b32 s20, 8, 0
	s_or_b32 s76, s76, s20
	v_cmp_ne_u64_e32 vcc, -1, v[8:9]
	s_and_b64 s[20:21], s[0:1], vcc
	s_cmp_lg_u64 s[20:21], 0
	s_cselect_b32 s20, 8, 0
	s_or_b32 s77, s77, s20
	v_lshl_add_u64 v[4:5], v[4:5], 0, 8
	global_load_dword v180, v96, s[60:61] offset:2560 nt
	global_load_dword v181, v96, s[62:63] offset:2560 nt
	global_load_dword v182, v96, s[64:65] offset:2560 nt
	global_load_dword v183, v96, s[66:67] offset:2560 nt
	global_load_dword v184, v96, s[68:69] offset:2560 nt
	global_load_dword v185, v96, s[70:71] offset:2560 nt
	global_load_dword v186, v96, s[72:73] offset:2560 nt
	global_load_dword v187, v96, s[74:75] offset:2560 nt
	s_waitcnt vmcnt(52)
	v_cmp_ne_u32_e32 vcc, 0, v132
	s_nop 1
	v_mov_b32_e32 v2, vcc_lo
	v_mov_b32_e32 v9, vcc_hi
	v_cmp_ne_u32_e32 vcc, 0, v133
	v_cndmask_b32_e64 v2, 0, v2, s[22:23]
	v_cndmask_b32_e64 v9, 0, v9, s[22:23]
	v_mov_b32_e32 v11, vcc_hi
	v_mov_b32_e32 v14, vcc_lo
	v_cndmask_b32_e64 v9, v9, v11, s[6:7]
	v_cndmask_b32_e64 v2, v2, v14, s[6:7]
	v_cmp_ne_u32_e32 vcc, 0, v134
	s_nop 1
	v_mov_b32_e32 v11, vcc_lo
	v_mov_b32_e32 v14, vcc_hi
	v_cmp_ne_u32_e32 vcc, 0, v135
	v_cndmask_b32_e64 v2, v2, v11, s[8:9]
	v_cndmask_b32_e64 v9, v9, v14, s[8:9]
	v_mov_b32_e32 v11, vcc_hi
	v_mov_b32_e32 v14, vcc_lo
	v_cmp_ne_u32_e32 vcc, 0, v136
	v_cndmask_b32_e64 v9, v9, v11, s[10:11]
	v_cndmask_b32_e64 v2, v2, v14, s[10:11]
	v_mov_b32_e32 v11, vcc_lo
	v_mov_b32_e32 v12, vcc_hi
	v_cmp_ne_u32_e32 vcc, 0, v137
	v_cndmask_b32_e64 v2, v2, v11, s[12:13]
	v_cndmask_b32_e64 v9, v9, v12, s[12:13]
	v_mov_b32_e32 v11, vcc_hi
	v_mov_b32_e32 v12, vcc_lo
	v_cndmask_b32_e64 v9, v9, v11, s[14:15]
	v_cndmask_b32_e64 v2, v2, v12, s[14:15]
	v_cmp_ne_u32_e32 vcc, 0, v138
	s_nop 1
	v_mov_b32_e32 v10, vcc_lo
	v_mov_b32_e32 v11, vcc_hi
	v_cmp_ne_u32_e32 vcc, 0, v139
	v_cndmask_b32_e64 v2, v2, v10, s[16:17]
	v_cndmask_b32_e64 v8, v9, v11, s[16:17]
	v_mov_b32_e32 v9, vcc_hi
	v_mov_b32_e32 v10, vcc_lo
	v_cndmask_b32_e64 v9, v8, v9, s[18:19]
	v_cndmask_b32_e64 v8, v2, v10, s[18:19]
	s_mov_b64 s[2:3], exec
	s_mov_b64 exec, s[0:1]
	global_store_dwordx2 v[4:5], v[8:9], off
	s_mov_b64 exec, s[2:3]
	v_cmp_ne_u64_e32 vcc, 0, v[8:9]
	s_and_b64 s[20:21], s[0:1], vcc
	s_cmp_lg_u64 s[20:21], 0
	s_cselect_b32 s20, 16, 0
	s_or_b32 s76, s76, s20
	v_cmp_ne_u64_e32 vcc, -1, v[8:9]
	s_and_b64 s[20:21], s[0:1], vcc
	s_cmp_lg_u64 s[20:21], 0
	s_cselect_b32 s20, 16, 0
	s_or_b32 s77, s77, s20
	v_lshl_add_u64 v[4:5], v[4:5], 0, 8
	global_load_dword v188, v96, s[60:61] offset:2816 nt
	global_load_dword v189, v96, s[62:63] offset:2816 nt
	global_load_dword v190, v96, s[64:65] offset:2816 nt
	global_load_dword v191, v96, s[66:67] offset:2816 nt
	global_load_dword v192, v96, s[68:69] offset:2816 nt
	global_load_dword v193, v96, s[70:71] offset:2816 nt
	global_load_dword v194, v96, s[72:73] offset:2816 nt
	global_load_dword v195, v96, s[74:75] offset:2816 nt
	s_waitcnt vmcnt(53)
	v_cmp_ne_u32_e32 vcc, 0, v140
	s_nop 1
	v_mov_b32_e32 v2, vcc_lo
	v_mov_b32_e32 v9, vcc_hi
	v_cmp_ne_u32_e32 vcc, 0, v141
	v_cndmask_b32_e64 v2, 0, v2, s[22:23]
	v_cndmask_b32_e64 v9, 0, v9, s[22:23]
	v_mov_b32_e32 v11, vcc_hi
	v_mov_b32_e32 v14, vcc_lo
	v_cndmask_b32_e64 v9, v9, v11, s[6:7]
	v_cndmask_b32_e64 v2, v2, v14, s[6:7]
	v_cmp_ne_u32_e32 vcc, 0, v142
	s_nop 1
	v_mov_b32_e32 v11, vcc_lo
	v_mov_b32_e32 v14, vcc_hi
	v_cmp_ne_u32_e32 vcc, 0, v143
	v_cndmask_b32_e64 v2, v2, v11, s[8:9]
	v_cndmask_b32_e64 v9, v9, v14, s[8:9]
	v_mov_b32_e32 v11, vcc_hi
	v_mov_b32_e32 v14, vcc_lo
	v_cmp_ne_u32_e32 vcc, 0, v144
	v_cndmask_b32_e64 v9, v9, v11, s[10:11]
	v_cndmask_b32_e64 v2, v2, v14, s[10:11]
	v_mov_b32_e32 v11, vcc_lo
	v_mov_b32_e32 v12, vcc_hi
	v_cmp_ne_u32_e32 vcc, 0, v145
	v_cndmask_b32_e64 v2, v2, v11, s[12:13]
	v_cndmask_b32_e64 v9, v9, v12, s[12:13]
	v_mov_b32_e32 v11, vcc_hi
	v_mov_b32_e32 v12, vcc_lo
	v_cndmask_b32_e64 v9, v9, v11, s[14:15]
	v_cndmask_b32_e64 v2, v2, v12, s[14:15]
	v_cmp_ne_u32_e32 vcc, 0, v146
	s_nop 1
	v_mov_b32_e32 v10, vcc_lo
	v_mov_b32_e32 v11, vcc_hi
	v_cmp_ne_u32_e32 vcc, 0, v147
	v_cndmask_b32_e64 v2, v2, v10, s[16:17]
	v_cndmask_b32_e64 v8, v9, v11, s[16:17]
	v_mov_b32_e32 v9, vcc_hi
	v_mov_b32_e32 v10, vcc_lo
	v_cndmask_b32_e64 v9, v8, v9, s[18:19]
	v_cndmask_b32_e64 v8, v2, v10, s[18:19]
	s_mov_b64 s[2:3], exec
	s_mov_b64 exec, s[0:1]
	global_store_dwordx2 v[4:5], v[8:9], off
	s_mov_b64 exec, s[2:3]
	v_cmp_ne_u64_e32 vcc, 0, v[8:9]
	s_and_b64 s[20:21], s[0:1], vcc
	s_cmp_lg_u64 s[20:21], 0
	s_cselect_b32 s20, 32, 0
	s_or_b32 s76, s76, s20
	v_cmp_ne_u64_e32 vcc, -1, v[8:9]
	s_and_b64 s[20:21], s[0:1], vcc
	s_cmp_lg_u64 s[20:21], 0
	s_cselect_b32 s20, 32, 0
	s_or_b32 s77, s77, s20
	v_lshl_add_u64 v[4:5], v[4:5], 0, 8
	global_load_dword v196, v96, s[60:61] offset:3072 nt
	global_load_dword v197, v96, s[62:63] offset:3072 nt
	global_load_dword v198, v96, s[64:65] offset:3072 nt
	global_load_dword v199, v96, s[66:67] offset:3072 nt
	global_load_dword v200, v96, s[68:69] offset:3072 nt
	global_load_dword v201, v96, s[70:71] offset:3072 nt
	global_load_dword v202, v96, s[72:73] offset:3072 nt
	global_load_dword v203, v96, s[74:75] offset:3072 nt
	s_waitcnt vmcnt(54)
	v_cmp_ne_u32_e32 vcc, 0, v148
	s_nop 1
	v_mov_b32_e32 v2, vcc_lo
	v_mov_b32_e32 v9, vcc_hi
	v_cmp_ne_u32_e32 vcc, 0, v149
	v_cndmask_b32_e64 v2, 0, v2, s[22:23]
	v_cndmask_b32_e64 v9, 0, v9, s[22:23]
	v_mov_b32_e32 v11, vcc_hi
	v_mov_b32_e32 v14, vcc_lo
	v_cndmask_b32_e64 v9, v9, v11, s[6:7]
	v_cndmask_b32_e64 v2, v2, v14, s[6:7]
	v_cmp_ne_u32_e32 vcc, 0, v150
	s_nop 1
	v_mov_b32_e32 v11, vcc_lo
	v_mov_b32_e32 v14, vcc_hi
	v_cmp_ne_u32_e32 vcc, 0, v151
	v_cndmask_b32_e64 v2, v2, v11, s[8:9]
	v_cndmask_b32_e64 v9, v9, v14, s[8:9]
	v_mov_b32_e32 v11, vcc_hi
	v_mov_b32_e32 v14, vcc_lo
	v_cmp_ne_u32_e32 vcc, 0, v152
	v_cndmask_b32_e64 v9, v9, v11, s[10:11]
	v_cndmask_b32_e64 v2, v2, v14, s[10:11]
	v_mov_b32_e32 v11, vcc_lo
	v_mov_b32_e32 v12, vcc_hi
	v_cmp_ne_u32_e32 vcc, 0, v153
	v_cndmask_b32_e64 v2, v2, v11, s[12:13]
	v_cndmask_b32_e64 v9, v9, v12, s[12:13]
	v_mov_b32_e32 v11, vcc_hi
	v_mov_b32_e32 v12, vcc_lo
	v_cndmask_b32_e64 v9, v9, v11, s[14:15]
	v_cndmask_b32_e64 v2, v2, v12, s[14:15]
	v_cmp_ne_u32_e32 vcc, 0, v154
	s_nop 1
	v_mov_b32_e32 v10, vcc_lo
	v_mov_b32_e32 v11, vcc_hi
	v_cmp_ne_u32_e32 vcc, 0, v155
	v_cndmask_b32_e64 v2, v2, v10, s[16:17]
	v_cndmask_b32_e64 v8, v9, v11, s[16:17]
	v_mov_b32_e32 v9, vcc_hi
	v_mov_b32_e32 v10, vcc_lo
	v_cndmask_b32_e64 v9, v8, v9, s[18:19]
	v_cndmask_b32_e64 v8, v2, v10, s[18:19]
	s_mov_b64 s[2:3], exec
	s_mov_b64 exec, s[0:1]
	global_store_dwordx2 v[4:5], v[8:9], off
	s_mov_b64 exec, s[2:3]
	v_cmp_ne_u64_e32 vcc, 0, v[8:9]
	s_and_b64 s[20:21], s[0:1], vcc
	s_cmp_lg_u64 s[20:21], 0
	s_cselect_b32 s20, 64, 0
	s_or_b32 s76, s76, s20
	v_cmp_ne_u64_e32 vcc, -1, v[8:9]
	s_and_b64 s[20:21], s[0:1], vcc
	s_cmp_lg_u64 s[20:21], 0
	s_cselect_b32 s20, 64, 0
	s_or_b32 s77, s77, s20
	v_lshl_add_u64 v[4:5], v[4:5], 0, 8
	global_load_dword v204, v96, s[60:61] offset:3328 nt
	global_load_dword v205, v96, s[62:63] offset:3328 nt
	global_load_dword v206, v96, s[64:65] offset:3328 nt
	global_load_dword v207, v96, s[66:67] offset:3328 nt
	global_load_dword v208, v96, s[68:69] offset:3328 nt
	global_load_dword v209, v96, s[70:71] offset:3328 nt
	global_load_dword v210, v96, s[72:73] offset:3328 nt
	global_load_dword v211, v96, s[74:75] offset:3328 nt
	s_waitcnt vmcnt(54)
	v_cmp_ne_u32_e32 vcc, 0, v156
	s_nop 1
	v_mov_b32_e32 v2, vcc_lo
	v_mov_b32_e32 v9, vcc_hi
	v_cmp_ne_u32_e32 vcc, 0, v157
	v_cndmask_b32_e64 v2, 0, v2, s[22:23]
	v_cndmask_b32_e64 v9, 0, v9, s[22:23]
	v_mov_b32_e32 v11, vcc_hi
	v_mov_b32_e32 v14, vcc_lo
	v_cndmask_b32_e64 v9, v9, v11, s[6:7]
	v_cndmask_b32_e64 v2, v2, v14, s[6:7]
	v_cmp_ne_u32_e32 vcc, 0, v158
	s_nop 1
	v_mov_b32_e32 v11, vcc_lo
	v_mov_b32_e32 v14, vcc_hi
	v_cmp_ne_u32_e32 vcc, 0, v159
	v_cndmask_b32_e64 v2, v2, v11, s[8:9]
	v_cndmask_b32_e64 v9, v9, v14, s[8:9]
	v_mov_b32_e32 v11, vcc_hi
	v_mov_b32_e32 v14, vcc_lo
	v_cmp_ne_u32_e32 vcc, 0, v160
	v_cndmask_b32_e64 v9, v9, v11, s[10:11]
	v_cndmask_b32_e64 v2, v2, v14, s[10:11]
	v_mov_b32_e32 v11, vcc_lo
	v_mov_b32_e32 v12, vcc_hi
	v_cmp_ne_u32_e32 vcc, 0, v161
	v_cndmask_b32_e64 v2, v2, v11, s[12:13]
	v_cndmask_b32_e64 v9, v9, v12, s[12:13]
	v_mov_b32_e32 v11, vcc_hi
	v_mov_b32_e32 v12, vcc_lo
	v_cndmask_b32_e64 v9, v9, v11, s[14:15]
	v_cndmask_b32_e64 v2, v2, v12, s[14:15]
	v_cmp_ne_u32_e32 vcc, 0, v162
	s_nop 1
	v_mov_b32_e32 v10, vcc_lo
	v_mov_b32_e32 v11, vcc_hi
	v_cmp_ne_u32_e32 vcc, 0, v163
	v_cndmask_b32_e64 v2, v2, v10, s[16:17]
	v_cndmask_b32_e64 v8, v9, v11, s[16:17]
	v_mov_b32_e32 v9, vcc_hi
	v_mov_b32_e32 v10, vcc_lo
	v_cndmask_b32_e64 v9, v8, v9, s[18:19]
	v_cndmask_b32_e64 v8, v2, v10, s[18:19]
	s_mov_b64 s[2:3], exec
	s_mov_b64 exec, s[0:1]
	global_store_dwordx2 v[4:5], v[8:9], off
	s_mov_b64 exec, s[2:3]
	v_cmp_ne_u64_e32 vcc, 0, v[8:9]
	s_and_b64 s[20:21], s[0:1], vcc
	s_cmp_lg_u64 s[20:21], 0
	s_cselect_b32 s20, 128, 0
	s_or_b32 s76, s76, s20
	v_cmp_ne_u64_e32 vcc, -1, v[8:9]
	s_and_b64 s[20:21], s[0:1], vcc
	s_cmp_lg_u64 s[20:21], 0
	s_cselect_b32 s20, 128, 0
	s_or_b32 s77, s77, s20
	v_lshl_add_u64 v[4:5], v[4:5], 0, 8
	global_load_dword v212, v96, s[60:61] offset:3584 nt
	global_load_dword v213, v96, s[62:63] offset:3584 nt
	global_load_dword v214, v96, s[64:65] offset:3584 nt
	global_load_dword v215, v96, s[66:67] offset:3584 nt
	global_load_dword v216, v96, s[68:69] offset:3584 nt
	global_load_dword v217, v96, s[70:71] offset:3584 nt
	global_load_dword v218, v96, s[72:73] offset:3584 nt
	global_load_dword v219, v96, s[74:75] offset:3584 nt
	s_waitcnt vmcnt(54)
	v_cmp_ne_u32_e32 vcc, 0, v164
	s_nop 1
	v_mov_b32_e32 v2, vcc_lo
	v_mov_b32_e32 v9, vcc_hi
	v_cmp_ne_u32_e32 vcc, 0, v165
	v_cndmask_b32_e64 v2, 0, v2, s[22:23]
	v_cndmask_b32_e64 v9, 0, v9, s[22:23]
	v_mov_b32_e32 v11, vcc_hi
	v_mov_b32_e32 v14, vcc_lo
	v_cndmask_b32_e64 v9, v9, v11, s[6:7]
	v_cndmask_b32_e64 v2, v2, v14, s[6:7]
	v_cmp_ne_u32_e32 vcc, 0, v166
	s_nop 1
	v_mov_b32_e32 v11, vcc_lo
	v_mov_b32_e32 v14, vcc_hi
	v_cmp_ne_u32_e32 vcc, 0, v167
	v_cndmask_b32_e64 v2, v2, v11, s[8:9]
	v_cndmask_b32_e64 v9, v9, v14, s[8:9]
	v_mov_b32_e32 v11, vcc_hi
	v_mov_b32_e32 v14, vcc_lo
	v_cmp_ne_u32_e32 vcc, 0, v168
	v_cndmask_b32_e64 v9, v9, v11, s[10:11]
	v_cndmask_b32_e64 v2, v2, v14, s[10:11]
	v_mov_b32_e32 v11, vcc_lo
	v_mov_b32_e32 v12, vcc_hi
	v_cmp_ne_u32_e32 vcc, 0, v169
	v_cndmask_b32_e64 v2, v2, v11, s[12:13]
	v_cndmask_b32_e64 v9, v9, v12, s[12:13]
	v_mov_b32_e32 v11, vcc_hi
	v_mov_b32_e32 v12, vcc_lo
	v_cndmask_b32_e64 v9, v9, v11, s[14:15]
	v_cndmask_b32_e64 v2, v2, v12, s[14:15]
	v_cmp_ne_u32_e32 vcc, 0, v170
	s_nop 1
	v_mov_b32_e32 v10, vcc_lo
	v_mov_b32_e32 v11, vcc_hi
	v_cmp_ne_u32_e32 vcc, 0, v171
	v_cndmask_b32_e64 v2, v2, v10, s[16:17]
	v_cndmask_b32_e64 v8, v9, v11, s[16:17]
	v_mov_b32_e32 v9, vcc_hi
	v_mov_b32_e32 v10, vcc_lo
	v_cndmask_b32_e64 v9, v8, v9, s[18:19]
	v_cndmask_b32_e64 v8, v2, v10, s[18:19]
	s_mov_b64 s[2:3], exec
	s_mov_b64 exec, s[0:1]
	global_store_dwordx2 v[4:5], v[8:9], off
	s_mov_b64 exec, s[2:3]
	v_cmp_ne_u64_e32 vcc, 0, v[8:9]
	s_and_b64 s[20:21], s[0:1], vcc
	s_cmp_lg_u64 s[20:21], 0
	s_cselect_b32 s20, 256, 0
	s_or_b32 s76, s76, s20
	v_cmp_ne_u64_e32 vcc, -1, v[8:9]
	s_and_b64 s[20:21], s[0:1], vcc
	s_cmp_lg_u64 s[20:21], 0
	s_cselect_b32 s20, 256, 0
	s_or_b32 s77, s77, s20
	v_lshl_add_u64 v[4:5], v[4:5], 0, 8
	global_load_dword v220, v96, s[60:61] offset:3840 nt
	global_load_dword v221, v96, s[62:63] offset:3840 nt
	global_load_dword v222, v96, s[64:65] offset:3840 nt
	global_load_dword v223, v96, s[66:67] offset:3840 nt
	global_load_dword v224, v96, s[68:69] offset:3840 nt
	global_load_dword v225, v96, s[70:71] offset:3840 nt
	global_load_dword v226, v96, s[72:73] offset:3840 nt
	global_load_dword v227, v96, s[74:75] offset:3840 nt
	s_waitcnt vmcnt(54)
	v_cmp_ne_u32_e32 vcc, 0, v172
	s_nop 1
	v_mov_b32_e32 v2, vcc_lo
	v_mov_b32_e32 v9, vcc_hi
	v_cmp_ne_u32_e32 vcc, 0, v173
	v_cndmask_b32_e64 v2, 0, v2, s[22:23]
	v_cndmask_b32_e64 v9, 0, v9, s[22:23]
	v_mov_b32_e32 v11, vcc_hi
	v_mov_b32_e32 v14, vcc_lo
	v_cndmask_b32_e64 v9, v9, v11, s[6:7]
	v_cndmask_b32_e64 v2, v2, v14, s[6:7]
	v_cmp_ne_u32_e32 vcc, 0, v174
	s_nop 1
	v_mov_b32_e32 v11, vcc_lo
	v_mov_b32_e32 v14, vcc_hi
	v_cmp_ne_u32_e32 vcc, 0, v175
	v_cndmask_b32_e64 v2, v2, v11, s[8:9]
	v_cndmask_b32_e64 v9, v9, v14, s[8:9]
	v_mov_b32_e32 v11, vcc_hi
	v_mov_b32_e32 v14, vcc_lo
	v_cmp_ne_u32_e32 vcc, 0, v176
	v_cndmask_b32_e64 v9, v9, v11, s[10:11]
	v_cndmask_b32_e64 v2, v2, v14, s[10:11]
	v_mov_b32_e32 v11, vcc_lo
	v_mov_b32_e32 v12, vcc_hi
	v_cmp_ne_u32_e32 vcc, 0, v177
	v_cndmask_b32_e64 v2, v2, v11, s[12:13]
	v_cndmask_b32_e64 v9, v9, v12, s[12:13]
	v_mov_b32_e32 v11, vcc_hi
	v_mov_b32_e32 v12, vcc_lo
	v_cndmask_b32_e64 v9, v9, v11, s[14:15]
	v_cndmask_b32_e64 v2, v2, v12, s[14:15]
	v_cmp_ne_u32_e32 vcc, 0, v178
	s_nop 1
	v_mov_b32_e32 v10, vcc_lo
	v_mov_b32_e32 v11, vcc_hi
	v_cmp_ne_u32_e32 vcc, 0, v179
	v_cndmask_b32_e64 v2, v2, v10, s[16:17]
	v_cndmask_b32_e64 v8, v9, v11, s[16:17]
	v_mov_b32_e32 v9, vcc_hi
	v_mov_b32_e32 v10, vcc_lo
	v_cndmask_b32_e64 v9, v8, v9, s[18:19]
	v_cndmask_b32_e64 v8, v2, v10, s[18:19]
	s_mov_b64 s[2:3], exec
	s_mov_b64 exec, s[0:1]
	global_store_dwordx2 v[4:5], v[8:9], off
	s_mov_b64 exec, s[2:3]
	v_cmp_ne_u64_e32 vcc, 0, v[8:9]
	s_and_b64 s[20:21], s[0:1], vcc
	s_cmp_lg_u64 s[20:21], 0
	s_cselect_b32 s20, 512, 0
	s_or_b32 s76, s76, s20
	v_cmp_ne_u64_e32 vcc, -1, v[8:9]
	s_and_b64 s[20:21], s[0:1], vcc
	s_cmp_lg_u64 s[20:21], 0
	s_cselect_b32 s20, 512, 0
	s_or_b32 s77, s77, s20
	v_lshl_add_u64 v[4:5], v[4:5], 0, 8
	s_waitcnt vmcnt(46)
	v_cmp_ne_u32_e32 vcc, 0, v180
	s_nop 1
	v_mov_b32_e32 v2, vcc_lo
	v_mov_b32_e32 v9, vcc_hi
	v_cmp_ne_u32_e32 vcc, 0, v181
	v_cndmask_b32_e64 v2, 0, v2, s[22:23]
	v_cndmask_b32_e64 v9, 0, v9, s[22:23]
	v_mov_b32_e32 v11, vcc_hi
	v_mov_b32_e32 v14, vcc_lo
	v_cndmask_b32_e64 v9, v9, v11, s[6:7]
	v_cndmask_b32_e64 v2, v2, v14, s[6:7]
	v_cmp_ne_u32_e32 vcc, 0, v182
	s_nop 1
	v_mov_b32_e32 v11, vcc_lo
	v_mov_b32_e32 v14, vcc_hi
	v_cmp_ne_u32_e32 vcc, 0, v183
	v_cndmask_b32_e64 v2, v2, v11, s[8:9]
	v_cndmask_b32_e64 v9, v9, v14, s[8:9]
	v_mov_b32_e32 v11, vcc_hi
	v_mov_b32_e32 v14, vcc_lo
	v_cmp_ne_u32_e32 vcc, 0, v184
	v_cndmask_b32_e64 v9, v9, v11, s[10:11]
	v_cndmask_b32_e64 v2, v2, v14, s[10:11]
	v_mov_b32_e32 v11, vcc_lo
	v_mov_b32_e32 v12, vcc_hi
	v_cmp_ne_u32_e32 vcc, 0, v185
	v_cndmask_b32_e64 v2, v2, v11, s[12:13]
	v_cndmask_b32_e64 v9, v9, v12, s[12:13]
	v_mov_b32_e32 v11, vcc_hi
	v_mov_b32_e32 v12, vcc_lo
	v_cndmask_b32_e64 v9, v9, v11, s[14:15]
	v_cndmask_b32_e64 v2, v2, v12, s[14:15]
	v_cmp_ne_u32_e32 vcc, 0, v186
	s_nop 1
	v_mov_b32_e32 v10, vcc_lo
	v_mov_b32_e32 v11, vcc_hi
	v_cmp_ne_u32_e32 vcc, 0, v187
	v_cndmask_b32_e64 v2, v2, v10, s[16:17]
	v_cndmask_b32_e64 v8, v9, v11, s[16:17]
	v_mov_b32_e32 v9, vcc_hi
	v_mov_b32_e32 v10, vcc_lo
	v_cndmask_b32_e64 v9, v8, v9, s[18:19]
	v_cndmask_b32_e64 v8, v2, v10, s[18:19]
	s_mov_b64 s[2:3], exec
	s_mov_b64 exec, s[0:1]
	global_store_dwordx2 v[4:5], v[8:9], off
	s_mov_b64 exec, s[2:3]
	v_cmp_ne_u64_e32 vcc, 0, v[8:9]
	s_and_b64 s[20:21], s[0:1], vcc
	s_cmp_lg_u64 s[20:21], 0
	s_cselect_b32 s20, 1024, 0
	s_or_b32 s76, s76, s20
	v_cmp_ne_u64_e32 vcc, -1, v[8:9]
	s_and_b64 s[20:21], s[0:1], vcc
	s_cmp_lg_u64 s[20:21], 0
	s_cselect_b32 s20, 1024, 0
	s_or_b32 s77, s77, s20
	v_lshl_add_u64 v[4:5], v[4:5], 0, 8
	s_waitcnt vmcnt(38)
	v_cmp_ne_u32_e32 vcc, 0, v188
	s_nop 1
	v_mov_b32_e32 v2, vcc_lo
	v_mov_b32_e32 v9, vcc_hi
	v_cmp_ne_u32_e32 vcc, 0, v189
	v_cndmask_b32_e64 v2, 0, v2, s[22:23]
	v_cndmask_b32_e64 v9, 0, v9, s[22:23]
	v_mov_b32_e32 v11, vcc_hi
	v_mov_b32_e32 v14, vcc_lo
	v_cndmask_b32_e64 v9, v9, v11, s[6:7]
	v_cndmask_b32_e64 v2, v2, v14, s[6:7]
	v_cmp_ne_u32_e32 vcc, 0, v190
	s_nop 1
	v_mov_b32_e32 v11, vcc_lo
	v_mov_b32_e32 v14, vcc_hi
	v_cmp_ne_u32_e32 vcc, 0, v191
	v_cndmask_b32_e64 v2, v2, v11, s[8:9]
	v_cndmask_b32_e64 v9, v9, v14, s[8:9]
	v_mov_b32_e32 v11, vcc_hi
	v_mov_b32_e32 v14, vcc_lo
	v_cmp_ne_u32_e32 vcc, 0, v192
	v_cndmask_b32_e64 v9, v9, v11, s[10:11]
	v_cndmask_b32_e64 v2, v2, v14, s[10:11]
	v_mov_b32_e32 v11, vcc_lo
	v_mov_b32_e32 v12, vcc_hi
	v_cmp_ne_u32_e32 vcc, 0, v193
	v_cndmask_b32_e64 v2, v2, v11, s[12:13]
	v_cndmask_b32_e64 v9, v9, v12, s[12:13]
	v_mov_b32_e32 v11, vcc_hi
	v_mov_b32_e32 v12, vcc_lo
	v_cndmask_b32_e64 v9, v9, v11, s[14:15]
	v_cndmask_b32_e64 v2, v2, v12, s[14:15]
	v_cmp_ne_u32_e32 vcc, 0, v194
	s_nop 1
	v_mov_b32_e32 v10, vcc_lo
	v_mov_b32_e32 v11, vcc_hi
	v_cmp_ne_u32_e32 vcc, 0, v195
	v_cndmask_b32_e64 v2, v2, v10, s[16:17]
	v_cndmask_b32_e64 v8, v9, v11, s[16:17]
	v_mov_b32_e32 v9, vcc_hi
	v_mov_b32_e32 v10, vcc_lo
	v_cndmask_b32_e64 v9, v8, v9, s[18:19]
	v_cndmask_b32_e64 v8, v2, v10, s[18:19]
	s_mov_b64 s[2:3], exec
	s_mov_b64 exec, s[0:1]
	global_store_dwordx2 v[4:5], v[8:9], off
	s_mov_b64 exec, s[2:3]
	v_cmp_ne_u64_e32 vcc, 0, v[8:9]
	s_and_b64 s[20:21], s[0:1], vcc
	s_cmp_lg_u64 s[20:21], 0
	s_cselect_b32 s20, 2048, 0
	s_or_b32 s76, s76, s20
	v_cmp_ne_u64_e32 vcc, -1, v[8:9]
	s_and_b64 s[20:21], s[0:1], vcc
	s_cmp_lg_u64 s[20:21], 0
	s_cselect_b32 s20, 2048, 0
	s_or_b32 s77, s77, s20
	v_lshl_add_u64 v[4:5], v[4:5], 0, 8
	s_waitcnt vmcnt(30)
	v_cmp_ne_u32_e32 vcc, 0, v196
	s_nop 1
	v_mov_b32_e32 v2, vcc_lo
	v_mov_b32_e32 v9, vcc_hi
	v_cmp_ne_u32_e32 vcc, 0, v197
	v_cndmask_b32_e64 v2, 0, v2, s[22:23]
	v_cndmask_b32_e64 v9, 0, v9, s[22:23]
	v_mov_b32_e32 v11, vcc_hi
	v_mov_b32_e32 v14, vcc_lo
	v_cndmask_b32_e64 v9, v9, v11, s[6:7]
	v_cndmask_b32_e64 v2, v2, v14, s[6:7]
	v_cmp_ne_u32_e32 vcc, 0, v198
	s_nop 1
	v_mov_b32_e32 v11, vcc_lo
	v_mov_b32_e32 v14, vcc_hi
	v_cmp_ne_u32_e32 vcc, 0, v199
	v_cndmask_b32_e64 v2, v2, v11, s[8:9]
	v_cndmask_b32_e64 v9, v9, v14, s[8:9]
	v_mov_b32_e32 v11, vcc_hi
	v_mov_b32_e32 v14, vcc_lo
	v_cmp_ne_u32_e32 vcc, 0, v200
	v_cndmask_b32_e64 v9, v9, v11, s[10:11]
	v_cndmask_b32_e64 v2, v2, v14, s[10:11]
	v_mov_b32_e32 v11, vcc_lo
	v_mov_b32_e32 v12, vcc_hi
	v_cmp_ne_u32_e32 vcc, 0, v201
	v_cndmask_b32_e64 v2, v2, v11, s[12:13]
	v_cndmask_b32_e64 v9, v9, v12, s[12:13]
	v_mov_b32_e32 v11, vcc_hi
	v_mov_b32_e32 v12, vcc_lo
	v_cndmask_b32_e64 v9, v9, v11, s[14:15]
	v_cndmask_b32_e64 v2, v2, v12, s[14:15]
	v_cmp_ne_u32_e32 vcc, 0, v202
	s_nop 1
	v_mov_b32_e32 v10, vcc_lo
	v_mov_b32_e32 v11, vcc_hi
	v_cmp_ne_u32_e32 vcc, 0, v203
	v_cndmask_b32_e64 v2, v2, v10, s[16:17]
	v_cndmask_b32_e64 v8, v9, v11, s[16:17]
	v_mov_b32_e32 v9, vcc_hi
	v_mov_b32_e32 v10, vcc_lo
	v_cndmask_b32_e64 v9, v8, v9, s[18:19]
	v_cndmask_b32_e64 v8, v2, v10, s[18:19]
	s_mov_b64 s[2:3], exec
	s_mov_b64 exec, s[0:1]
	global_store_dwordx2 v[4:5], v[8:9], off
	s_mov_b64 exec, s[2:3]
	v_cmp_ne_u64_e32 vcc, 0, v[8:9]
	s_and_b64 s[20:21], s[0:1], vcc
	s_cmp_lg_u64 s[20:21], 0
	s_cselect_b32 s20, 4096, 0
	s_or_b32 s76, s76, s20
	v_cmp_ne_u64_e32 vcc, -1, v[8:9]
	s_and_b64 s[20:21], s[0:1], vcc
	s_cmp_lg_u64 s[20:21], 0
	s_cselect_b32 s20, 4096, 0
	s_or_b32 s77, s77, s20
	v_lshl_add_u64 v[4:5], v[4:5], 0, 8
	s_waitcnt vmcnt(22)
	v_cmp_ne_u32_e32 vcc, 0, v204
	s_nop 1
	v_mov_b32_e32 v2, vcc_lo
	v_mov_b32_e32 v9, vcc_hi
	v_cmp_ne_u32_e32 vcc, 0, v205
	v_cndmask_b32_e64 v2, 0, v2, s[22:23]
	v_cndmask_b32_e64 v9, 0, v9, s[22:23]
	v_mov_b32_e32 v11, vcc_hi
	v_mov_b32_e32 v14, vcc_lo
	v_cndmask_b32_e64 v9, v9, v11, s[6:7]
	v_cndmask_b32_e64 v2, v2, v14, s[6:7]
	v_cmp_ne_u32_e32 vcc, 0, v206
	s_nop 1
	v_mov_b32_e32 v11, vcc_lo
	v_mov_b32_e32 v14, vcc_hi
	v_cmp_ne_u32_e32 vcc, 0, v207
	v_cndmask_b32_e64 v2, v2, v11, s[8:9]
	v_cndmask_b32_e64 v9, v9, v14, s[8:9]
	v_mov_b32_e32 v11, vcc_hi
	v_mov_b32_e32 v14, vcc_lo
	v_cmp_ne_u32_e32 vcc, 0, v208
	v_cndmask_b32_e64 v9, v9, v11, s[10:11]
	v_cndmask_b32_e64 v2, v2, v14, s[10:11]
	v_mov_b32_e32 v11, vcc_lo
	v_mov_b32_e32 v12, vcc_hi
	v_cmp_ne_u32_e32 vcc, 0, v209
	v_cndmask_b32_e64 v2, v2, v11, s[12:13]
	v_cndmask_b32_e64 v9, v9, v12, s[12:13]
	v_mov_b32_e32 v11, vcc_hi
	v_mov_b32_e32 v12, vcc_lo
	v_cndmask_b32_e64 v9, v9, v11, s[14:15]
	v_cndmask_b32_e64 v2, v2, v12, s[14:15]
	v_cmp_ne_u32_e32 vcc, 0, v210
	s_nop 1
	v_mov_b32_e32 v10, vcc_lo
	v_mov_b32_e32 v11, vcc_hi
	v_cmp_ne_u32_e32 vcc, 0, v211
	v_cndmask_b32_e64 v2, v2, v10, s[16:17]
	v_cndmask_b32_e64 v8, v9, v11, s[16:17]
	v_mov_b32_e32 v9, vcc_hi
	v_mov_b32_e32 v10, vcc_lo
	v_cndmask_b32_e64 v9, v8, v9, s[18:19]
	v_cndmask_b32_e64 v8, v2, v10, s[18:19]
	s_mov_b64 s[2:3], exec
	s_mov_b64 exec, s[0:1]
	global_store_dwordx2 v[4:5], v[8:9], off
	s_mov_b64 exec, s[2:3]
	v_cmp_ne_u64_e32 vcc, 0, v[8:9]
	s_and_b64 s[20:21], s[0:1], vcc
	s_cmp_lg_u64 s[20:21], 0
	s_cselect_b32 s20, 8192, 0
	s_or_b32 s76, s76, s20
	v_cmp_ne_u64_e32 vcc, -1, v[8:9]
	s_and_b64 s[20:21], s[0:1], vcc
	s_cmp_lg_u64 s[20:21], 0
	s_cselect_b32 s20, 8192, 0
	s_or_b32 s77, s77, s20
	v_lshl_add_u64 v[4:5], v[4:5], 0, 8
	s_waitcnt vmcnt(14)
	v_cmp_ne_u32_e32 vcc, 0, v212
	s_nop 1
	v_mov_b32_e32 v2, vcc_lo
	v_mov_b32_e32 v9, vcc_hi
	v_cmp_ne_u32_e32 vcc, 0, v213
	v_cndmask_b32_e64 v2, 0, v2, s[22:23]
	v_cndmask_b32_e64 v9, 0, v9, s[22:23]
	v_mov_b32_e32 v11, vcc_hi
	v_mov_b32_e32 v14, vcc_lo
	v_cndmask_b32_e64 v9, v9, v11, s[6:7]
	v_cndmask_b32_e64 v2, v2, v14, s[6:7]
	v_cmp_ne_u32_e32 vcc, 0, v214
	s_nop 1
	v_mov_b32_e32 v11, vcc_lo
	v_mov_b32_e32 v14, vcc_hi
	v_cmp_ne_u32_e32 vcc, 0, v215
	v_cndmask_b32_e64 v2, v2, v11, s[8:9]
	v_cndmask_b32_e64 v9, v9, v14, s[8:9]
	v_mov_b32_e32 v11, vcc_hi
	v_mov_b32_e32 v14, vcc_lo
	v_cmp_ne_u32_e32 vcc, 0, v216
	v_cndmask_b32_e64 v9, v9, v11, s[10:11]
	v_cndmask_b32_e64 v2, v2, v14, s[10:11]
	v_mov_b32_e32 v11, vcc_lo
	v_mov_b32_e32 v12, vcc_hi
	v_cmp_ne_u32_e32 vcc, 0, v217
	v_cndmask_b32_e64 v2, v2, v11, s[12:13]
	v_cndmask_b32_e64 v9, v9, v12, s[12:13]
	v_mov_b32_e32 v11, vcc_hi
	v_mov_b32_e32 v12, vcc_lo
	v_cndmask_b32_e64 v9, v9, v11, s[14:15]
	v_cndmask_b32_e64 v2, v2, v12, s[14:15]
	v_cmp_ne_u32_e32 vcc, 0, v218
	s_nop 1
	v_mov_b32_e32 v10, vcc_lo
	v_mov_b32_e32 v11, vcc_hi
	v_cmp_ne_u32_e32 vcc, 0, v219
	v_cndmask_b32_e64 v2, v2, v10, s[16:17]
	v_cndmask_b32_e64 v8, v9, v11, s[16:17]
	v_mov_b32_e32 v9, vcc_hi
	v_mov_b32_e32 v10, vcc_lo
	v_cndmask_b32_e64 v9, v8, v9, s[18:19]
	v_cndmask_b32_e64 v8, v2, v10, s[18:19]
	s_mov_b64 s[2:3], exec
	s_mov_b64 exec, s[0:1]
	global_store_dwordx2 v[4:5], v[8:9], off
	s_mov_b64 exec, s[2:3]
	v_cmp_ne_u64_e32 vcc, 0, v[8:9]
	s_and_b64 s[20:21], s[0:1], vcc
	s_cmp_lg_u64 s[20:21], 0
	s_cselect_b32 s20, 16384, 0
	s_or_b32 s76, s76, s20
	v_cmp_ne_u64_e32 vcc, -1, v[8:9]
	s_and_b64 s[20:21], s[0:1], vcc
	s_cmp_lg_u64 s[20:21], 0
	s_cselect_b32 s20, 16384, 0
	s_or_b32 s77, s77, s20
	v_lshl_add_u64 v[4:5], v[4:5], 0, 8
	s_waitcnt vmcnt(6)
	v_cmp_ne_u32_e32 vcc, 0, v220
	s_nop 1
	v_mov_b32_e32 v2, vcc_lo
	v_mov_b32_e32 v9, vcc_hi
	v_cmp_ne_u32_e32 vcc, 0, v221
	v_cndmask_b32_e64 v2, 0, v2, s[22:23]
	v_cndmask_b32_e64 v9, 0, v9, s[22:23]
	v_mov_b32_e32 v11, vcc_hi
	v_mov_b32_e32 v14, vcc_lo
	v_cndmask_b32_e64 v9, v9, v11, s[6:7]
	v_cndmask_b32_e64 v2, v2, v14, s[6:7]
	v_cmp_ne_u32_e32 vcc, 0, v222
	s_nop 1
	v_mov_b32_e32 v11, vcc_lo
	v_mov_b32_e32 v14, vcc_hi
	v_cmp_ne_u32_e32 vcc, 0, v223
	v_cndmask_b32_e64 v2, v2, v11, s[8:9]
	v_cndmask_b32_e64 v9, v9, v14, s[8:9]
	v_mov_b32_e32 v11, vcc_hi
	v_mov_b32_e32 v14, vcc_lo
	v_cmp_ne_u32_e32 vcc, 0, v224
	v_cndmask_b32_e64 v9, v9, v11, s[10:11]
	v_cndmask_b32_e64 v2, v2, v14, s[10:11]
	v_mov_b32_e32 v11, vcc_lo
	v_mov_b32_e32 v12, vcc_hi
	v_cmp_ne_u32_e32 vcc, 0, v225
	v_cndmask_b32_e64 v2, v2, v11, s[12:13]
	v_cndmask_b32_e64 v9, v9, v12, s[12:13]
	v_mov_b32_e32 v11, vcc_hi
	v_mov_b32_e32 v12, vcc_lo
	v_cndmask_b32_e64 v9, v9, v11, s[14:15]
	v_cndmask_b32_e64 v2, v2, v12, s[14:15]
	v_cmp_ne_u32_e32 vcc, 0, v226
	s_nop 1
	v_mov_b32_e32 v10, vcc_lo
	v_mov_b32_e32 v11, vcc_hi
	v_cmp_ne_u32_e32 vcc, 0, v227
	v_cndmask_b32_e64 v2, v2, v10, s[16:17]
	v_cndmask_b32_e64 v8, v9, v11, s[16:17]
	v_mov_b32_e32 v9, vcc_hi
	v_mov_b32_e32 v10, vcc_lo
	v_cndmask_b32_e64 v9, v8, v9, s[18:19]
	v_cndmask_b32_e64 v8, v2, v10, s[18:19]
	s_mov_b64 s[2:3], exec
	s_mov_b64 exec, s[0:1]
	global_store_dwordx2 v[4:5], v[8:9], off
	s_mov_b64 exec, s[2:3]
	v_cmp_ne_u64_e32 vcc, 0, v[8:9]
	s_and_b64 s[20:21], s[0:1], vcc
	s_cmp_lg_u64 s[20:21], 0
	s_cselect_b32 s20, 32768, 0
	s_or_b32 s76, s76, s20
	v_cmp_ne_u64_e32 vcc, -1, v[8:9]
	s_and_b64 s[20:21], s[0:1], vcc
	s_cmp_lg_u64 s[20:21], 0
	s_cselect_b32 s20, 32768, 0
	s_or_b32 s77, s77, s20
	v_lshl_add_u64 v[4:5], v[4:5], 0, 8
	v_mov_b32_e32 v2, s76
	v_mov_b32_e32 v8, s77
	s_mov_b64 s[2:3], exec
	s_mov_b64 exec, s[22:23]
	ds_write2_b32 v1, v2, v8 offset1:8
	s_mov_b64 exec, s[2:3]
	s_waitcnt lgkmcnt(0)
	s_barrier
	ds_read_b128 v[8:11], v3
	ds_read_b128 v[12:15], v3 offset:16
	ds_read_b128 v[16:19], v3 offset:32
	ds_read_b128 v[20:23], v3 offset:48
	s_waitcnt lgkmcnt(0)
	v_or_b32_e32 v8, v8, v9
	v_or3_b32 v8, v8, v10, v11
	v_or3_b32 v8, v8, v12, v13
	v_or3_b32 v8, v8, v14, v15
	v_or_b32_e32 v16, v16, v17
	v_or3_b32 v16, v16, v18, v19
	v_or3_b32 v16, v16, v20, v21
	v_or3_b32 v16, v16, v22, v23
	v_and_b32_e32 v2, 15, v0
	v_lshrrev_b32_e32 v8, v2, v8
	v_and_b32_e32 v8, 1, v8
	v_lshrrev_b32_e32 v16, v2, v16
	v_and_b32_e32 v16, 1, v16
	v_lshl_or_b32 v8, v16, 1, v8
	v_lshlrev_b32_e32 v2, 2, v2
	v_cmp_gt_u32_e32 vcc, 16, v0
	s_and_saveexec_b64 s[2:3], vcc
	global_store_dword v2, v8, s[26:27]
	s_mov_b64 exec, s[2:3]
